# baseline (speedup 1.0000x reference)
.LBB0_2:
	s_or_b64 exec, exec, s[2:3]
	s_load_dwordx2 s[2:3], s[0:1], 0x10
	s_load_dwordx4 s[4:7], s[0:1], 0x20
	s_movk_i32 s10, 0x108
	v_mul_u32_u24_e32 v11, 0x108, v14
	v_mad_u32_u24 v14, v14, s10, v10
	s_waitcnt vmcnt(0)
	ds_write2_b64 v14, v[6:7], v[8:9] offset1:1
	s_and_saveexec_b64 s[0:1], vcc
	v_mul_u32_u24_e32 v6, 0x108, v0
	ds_write2_b64 v6, v[2:3], v[4:5] offset0:16 offset1:17
	s_or_b64 exec, exec, s[0:1]
	s_lshr_b32 s0, s11, 1
	v_mov_b32_e32 v3, 0
	s_and_b32 s0, s0, 0x7fffffe0
	v_and_b32_e32 v9, 15, v0
	v_or_b32_e32 v6, s0, v9
	v_mov_b32_e32 v7, v3
	v_lshl_add_u64 v[6:7], v[6:7], 2, s[8:9]
	v_bfe_u32 v8, v0, 4, 2
	global_load_dword a0, v[6:7], off
	v_lshlrev_b32_e32 v2, 8, v8
	s_mov_b32 s1, 0
	s_waitcnt lgkmcnt(0)
	v_lshl_add_u64 v[4:5], s[2:3], 0, v[2:3]
	v_lshl_add_u64 v[4:5], s[0:1], 2, v[4:5]
	v_lshlrev_b32_e32 v2, 2, v9
	v_lshl_add_u64 v[4:5], v[4:5], 0, v[2:3]
	global_load_dword v0, v[4:5], off
	global_load_dword a4, v[6:7], off offset:64
	global_load_dword v14, v[4:5], off offset:64
	global_load_dword v15, v[4:5], off offset:1024
	global_load_dword v16, v[4:5], off offset:1088
	global_load_dword v17, v[4:5], off offset:2048
	global_load_dword v18, v[4:5], off offset:2112
	global_load_dword v20, v[4:5], off offset:3072
	global_load_dword v21, v[4:5], off offset:3136
	s_movk_i32 s1, 0x1000
	v_lshlrev_b32_e32 v6, 2, v8
	v_mad_u32_u24 v19, v9, s10, v6
	v_add_co_u32_e32 v6, vcc, s1, v4
	s_movk_i32 s2, 0x2000
	s_nop 0
	v_addc_co_u32_e32 v7, vcc, 0, v5, vcc
	v_add_co_u32_e32 v4, vcc, s2, v4
	v_mul_u32_u24_e32 v8, 0x108, v8
	s_nop 0
	v_addc_co_u32_e32 v5, vcc, 0, v5, vcc
	global_load_dword v22, v[6:7], off offset:64
	global_load_dword v23, v[6:7], off offset:1024
	global_load_dword v24, v[6:7], off offset:1088
	global_load_dword v25, v[6:7], off offset:2048
	global_load_dword v26, v[6:7], off offset:2112
	global_load_dword v27, v[6:7], off offset:3072
	global_load_dword v28, v[6:7], off offset:3136
	global_load_dword v29, v[4:5], off offset:-4096
	global_load_dword v30, v[4:5], off
	global_load_dword v31, v[4:5], off offset:64
	s_barrier
	ds_read2_b32 v[4:5], v19 offset1:4
	v_lshl_add_u64 v[6:7], s[6:7], 0, v[12:13]
	v_add_lshl_u32 v8, v8, s0, 2
	v_add_u32_e32 v2, v8, v2
	s_waitcnt vmcnt(19)
	v_accvgpr_mov_b32 a1, a0
	v_accvgpr_mov_b32 a2, a0
	v_accvgpr_mov_b32 a3, a0
	s_waitcnt vmcnt(17)
	v_accvgpr_mov_b32 a5, a4
	v_accvgpr_mov_b32 a6, a4
	v_accvgpr_mov_b32 a7, a4
	s_waitcnt lgkmcnt(0)
	v_mfma_f32_16x16x4_f32 a[0:3], v4, v0, a[0:3]
	s_waitcnt vmcnt(16)
	v_mfma_f32_16x16x4_f32 a[4:7], v4, v14, a[4:7]
	v_lshl_add_u32 v14, v1, 5, v11
	v_lshl_add_u64 v[0:1], s[4:5], 0, v[12:13]
	ds_read_b32 v12, v19 offset:128
	v_mul_u32_u24_e32 v13, 0x108, v9
	v_mul_i32_i24_e32 v9, 0xfffffefc, v9
	v_mov_b32_e32 v11, v3
	v_lshl_add_u64 v[0:1], v[0:1], 0, v[10:11]
	s_waitcnt vmcnt(15)
	v_mfma_f32_16x16x4_f32 a[0:3], v5, v15, a[0:3]
	v_lshl_add_u64 v[10:11], v[6:7], 0, v[10:11]
	v_add3_u32 v6, v13, v9, v8
	s_waitcnt vmcnt(14)
	v_mfma_f32_16x16x4_f32 a[4:7], v5, v16, a[4:7]
	ds_read2_b32 v[4:5], v19 offset0:8 offset1:12
	s_waitcnt vmcnt(13) lgkmcnt(0)
	v_mfma_f32_16x16x4_f32 a[0:3], v4, v17, a[0:3]
	s_waitcnt vmcnt(12)
	v_mfma_f32_16x16x4_f32 a[4:7], v4, v18, a[4:7]
	s_waitcnt vmcnt(11)
	v_mfma_f32_16x16x4_f32 a[0:3], v5, v20, a[0:3]
	s_waitcnt vmcnt(10)
	v_mfma_f32_16x16x4_f32 a[4:7], v5, v21, a[4:7]
	ds_read2_b32 v[4:5], v19 offset0:16 offset1:20
	s_waitcnt vmcnt(2) lgkmcnt(0)
	v_mfma_f32_16x16x4_f32 a[0:3], v4, v29, a[0:3]
	v_mfma_f32_16x16x4_f32 a[4:7], v4, v22, a[4:7]
	v_mfma_f32_16x16x4_f32 a[0:3], v5, v23, a[0:3]
	v_mfma_f32_16x16x4_f32 a[4:7], v5, v24, a[4:7]
	ds_read2_b32 v[4:5], v19 offset0:24 offset1:28
	s_waitcnt lgkmcnt(0)
	s_barrier
	v_mfma_f32_16x16x4_f32 a[0:3], v4, v25, a[0:3]
	v_mfma_f32_16x16x4_f32 a[4:7], v4, v26, a[4:7]
	v_mov_b32_e32 v4, v3
	v_mfma_f32_16x16x4_f32 a[0:3], v5, v27, a[0:3]
	v_mfma_f32_16x16x4_f32 a[4:7], v5, v28, a[4:7]
	v_mov_b32_e32 v5, v3
	s_waitcnt vmcnt(1)
	v_mfma_f32_16x16x4_f32 a[0:3], v12, v30, a[0:3]
	s_waitcnt vmcnt(0)
	v_mfma_f32_16x16x4_f32 a[4:7], v12, v31, a[4:7]
	s_nop 7
	ds_write_b32 v6, a0
	s_nop 0
	ds_write_b32 v2, a4 offset:64
	ds_write_b32 v6, a1 offset:264
	ds_write_b32 v2, a5 offset:328
	ds_write_b32 v6, a2 offset:528
	ds_write_b32 v2, a6 offset:592
	ds_write_b32 v6, a3 offset:792
	ds_write_b32 v2, a7 offset:856
	s_waitcnt lgkmcnt(0)
	s_barrier
	ds_read2_b32 v[6:7], v14 offset1:7
	ds_read2_b32 v[8:9], v14 offset0:1 offset1:2
	ds_read2_b32 v[12:13], v14 offset0:3 offset1:4
	ds_read2_b32 v[14:15], v14 offset0:5 offset1:6
	v_mov_b32_e32 v2, v3
	s_waitcnt lgkmcnt(3)
	v_cvt_f16_f32_e32 v6, v6
	s_waitcnt lgkmcnt(2)
	v_cvt_pk_f16_f32 v9, v8, v9
	s_waitcnt lgkmcnt(1)
	v_cvt_pk_f16_f32 v8, v12, v13
	v_cvt_f16_f32_e32 v13, v7
	s_waitcnt lgkmcnt(0)
	v_cvt_pk_f16_f32 v12, v14, v15
	v_alignbit_b32 v7, v8, v9, 16
	v_alignbit_b32 v8, v12, v8, 16
	v_pack_b32_f16 v6, v6, v9
	v_alignbit_b32 v9, v13, v12, 16
	global_store_dwordx4 v[0:1], v[6:9], off
	global_store_dwordx4 v[10:11], v[2:5], off
	s_endpgm
	.p2align	8

.LBB1_10:
	s_endpgm
	.p2align	8

	.amdhsa_kernel _Z11edge_kernelILi36ELb1EEvPKfS1_PKDF16_PKiS5_S1_S1_S1_S1_S1_PDF16_
		.amdhsa_group_segment_fixed_size 16896
		.amdhsa_private_segment_fixed_size 0
		.amdhsa_kernarg_size 88
		.amdhsa_user_sgpr_count 2
		.amdhsa_user_sgpr_dispatch_ptr 0
		.amdhsa_user_sgpr_queue_ptr 0
		.amdhsa_user_sgpr_kernarg_segment_ptr 1
		.amdhsa_user_sgpr_dispatch_id 0
		.amdhsa_user_sgpr_kernarg_preload_length 0
		.amdhsa_user_sgpr_kernarg_preload_offset 0
		.amdhsa_user_sgpr_private_segment_size 0
		.amdhsa_uses_dynamic_stack 0
		.amdhsa_enable_private_segment 0
		.amdhsa_system_sgpr_workgroup_id_x 1
		.amdhsa_system_sgpr_workgroup_id_y 0
		.amdhsa_system_sgpr_workgroup_id_z 0
		.amdhsa_system_sgpr_workgroup_info 0
		.amdhsa_system_vgpr_workitem_id 0
		.amdhsa_next_free_vgpr 176
		.amdhsa_next_free_sgpr 96
		.amdhsa_accum_offset 140
		.amdhsa_reserve_vcc 1
		.amdhsa_float_round_mode_32 0
		.amdhsa_float_round_mode_16_64 0
		.amdhsa_float_denorm_mode_32 3
		.amdhsa_float_denorm_mode_16_64 3
		.amdhsa_dx10_clamp 1
		.amdhsa_ieee_mode 1
		.amdhsa_fp16_overflow 0
		.amdhsa_tg_split 0
		.amdhsa_exception_fp_ieee_invalid_op 0
		.amdhsa_exception_fp_denorm_src 0
		.amdhsa_exception_fp_ieee_div_zero 0
		.amdhsa_exception_fp_ieee_overflow 0
		.amdhsa_exception_fp_ieee_underflow 0
		.amdhsa_exception_fp_ieee_inexact 0
		.amdhsa_exception_int_div_zero 0
	.end_amdhsa_kernel

	.amdhsa_kernel _Z11edge_kernelILi64ELb0EEvPKfS1_PKDF16_PKiS5_S1_S1_S1_S1_S1_PDF16_
		.amdhsa_group_segment_fixed_size 16896
		.amdhsa_private_segment_fixed_size 0
		.amdhsa_kernarg_size 88
		.amdhsa_user_sgpr_count 2
		.amdhsa_user_sgpr_dispatch_ptr 0
		.amdhsa_user_sgpr_queue_ptr 0
		.amdhsa_user_sgpr_kernarg_segment_ptr 1
		.amdhsa_user_sgpr_dispatch_id 0
		.amdhsa_user_sgpr_kernarg_preload_length 0
		.amdhsa_user_sgpr_kernarg_preload_offset 0
		.amdhsa_user_sgpr_private_segment_size 0
		.amdhsa_uses_dynamic_stack 0
		.amdhsa_enable_private_segment 0
		.amdhsa_system_sgpr_workgroup_id_x 1
		.amdhsa_system_sgpr_workgroup_id_y 0
		.amdhsa_system_sgpr_workgroup_id_z 0
		.amdhsa_system_sgpr_workgroup_info 0
		.amdhsa_system_vgpr_workitem_id 0
		.amdhsa_next_free_vgpr 176
		.amdhsa_next_free_sgpr 96
		.amdhsa_accum_offset 168
		.amdhsa_reserve_vcc 1
		.amdhsa_float_round_mode_32 0
		.amdhsa_float_round_mode_16_64 0
		.amdhsa_float_denorm_mode_32 3
		.amdhsa_float_denorm_mode_16_64 3
		.amdhsa_dx10_clamp 1
		.amdhsa_ieee_mode 1
		.amdhsa_fp16_overflow 0
		.amdhsa_tg_split 0
		.amdhsa_exception_fp_ieee_invalid_op 0
		.amdhsa_exception_fp_denorm_src 0
		.amdhsa_exception_fp_ieee_div_zero 0
		.amdhsa_exception_fp_ieee_overflow 0
		.amdhsa_exception_fp_ieee_underflow 0
		.amdhsa_exception_fp_ieee_inexact 0
		.amdhsa_exception_int_div_zero 0
	.end_amdhsa_kernel

amdhsa.kernels:
  - .agpr_count:     8
    .args:
      - .actual_access:  read_only
        .address_space:  global
        .offset:         0
        .size:           8
        .value_kind:     global_buffer
      - .actual_access:  read_only
        .address_space:  global
        .offset:         8
        .size:           8
        .value_kind:     global_buffer
      - .actual_access:  read_only
        .address_space:  global
        .offset:         16
        .size:           8
        .value_kind:     global_buffer
      - .actual_access:  read_only
        .address_space:  global
        .offset:         24
        .size:           8
        .value_kind:     global_buffer
      - .actual_access:  write_only
        .address_space:  global
        .offset:         32
        .size:           8
        .value_kind:     global_buffer
      - .actual_access:  write_only
        .address_space:  global
        .offset:         40
        .size:           8
        .value_kind:     global_buffer
    .group_segment_fixed_size: 4224
    .kernarg_segment_align: 8
    .kernarg_segment_size: 48
    .language:       OpenCL C
    .language_version:
      - 2
      - 0
    .max_flat_workgroup_size: 128
    .name:           _Z11init_kernelPKfS0_S0_S0_PDF16_S1_
    .private_segment_fixed_size: 0
    .sgpr_count:     18
    .sgpr_spill_count: 0
    .symbol:         _Z11init_kernelPKfS0_S0_S0_PDF16_S1_.kd
    .uniform_work_group_size: 1
    .uses_dynamic_stack: false
    .vgpr_count:     40
    .vgpr_spill_count: 0
    .wavefront_size: 64
  - .agpr_count:     8
    .args:
      - .actual_access:  read_only
        .address_space:  global
        .offset:         0
        .size:           8
        .value_kind:     global_buffer
      - .actual_access:  read_only
        .address_space:  global
        .offset:         8
        .size:           8
        .value_kind:     global_buffer
      - .actual_access:  read_only
        .address_space:  global
        .offset:         16
        .size:           8
        .value_kind:     global_buffer
      - .actual_access:  read_only
        .address_space:  global
        .offset:         24
        .size:           8
        .value_kind:     global_buffer
      - .actual_access:  read_only
        .address_space:  global
        .offset:         32
        .size:           8
        .value_kind:     global_buffer
      - .actual_access:  read_only
        .address_space:  global
        .offset:         40
        .size:           8
        .value_kind:     global_buffer
      - .actual_access:  write_only
        .address_space:  global
        .offset:         48
        .size:           8
        .value_kind:     global_buffer
    .group_segment_fixed_size: 4352
    .kernarg_segment_align: 8
    .kernarg_segment_size: 56
    .language:       OpenCL C
    .language_version:
      - 2
      - 0
    .max_flat_workgroup_size: 128
    .name:           _Z12final_kernelPKDF16_S0_PKfS2_S2_S2_Pf
    .private_segment_fixed_size: 0
    .sgpr_count:     19
    .sgpr_spill_count: 0
    .symbol:         _Z12final_kernelPKDF16_S0_PKfS2_S2_S2_Pf.kd
    .uniform_work_group_size: 1
    .uses_dynamic_stack: false
    .vgpr_count:     60
    .vgpr_spill_count: 0
    .wavefront_size: 64
  - .agpr_count:     0
    .args:
      - .actual_access:  read_only
        .address_space:  global
        .offset:         0
        .size:           8
        .value_kind:     global_buffer
      - .actual_access:  read_only
        .address_space:  global
        .offset:         8
        .size:           8
        .value_kind:     global_buffer
      - .actual_access:  read_only
        .address_space:  global
        .offset:         16
        .size:           8
        .value_kind:     global_buffer
      - .actual_access:  read_only
        .address_space:  global
        .offset:         24
        .size:           8
        .value_kind:     global_buffer
      - .actual_access:  read_only
        .address_space:  global
        .offset:         32
        .size:           8
        .value_kind:     global_buffer
      - .actual_access:  read_only
        .address_space:  global
        .offset:         40
        .size:           8
        .value_kind:     global_buffer
      - .actual_access:  read_only
        .address_space:  global
        .offset:         48
        .size:           8
        .value_kind:     global_buffer
      - .actual_access:  read_only
        .address_space:  global
        .offset:         56
        .size:           8
        .value_kind:     global_buffer
      - .actual_access:  read_only
        .address_space:  global
        .offset:         64
        .size:           8
        .value_kind:     global_buffer
      - .actual_access:  read_only
        .address_space:  global
        .offset:         72
        .size:           8
        .value_kind:     global_buffer
      - .address_space:  global
        .offset:         80
        .size:           8
        .value_kind:     global_buffer
    .group_segment_fixed_size: 16896
    .kernarg_segment_align: 8
    .kernarg_segment_size: 88
    .language:       OpenCL C
    .language_version:
      - 2
      - 0
    .max_flat_workgroup_size: 128
    .name:           _Z11edge_kernelILi36ELb1EEvPKfS1_PKDF16_PKiS5_S1_S1_S1_S1_S1_PDF16_
    .private_segment_fixed_size: 0
    .sgpr_count:     23
    .sgpr_spill_count: 0
    .symbol:         _Z11edge_kernelILi36ELb1EEvPKfS1_PKDF16_PKiS5_S1_S1_S1_S1_S1_PDF16_.kd
    .uniform_work_group_size: 1
    .uses_dynamic_stack: false
    .vgpr_count:     176
    .vgpr_spill_count: 0
    .wavefront_size: 64
  - .agpr_count:     0
    .args:
      - .actual_access:  read_only
        .address_space:  global
        .offset:         0
        .size:           8
        .value_kind:     global_buffer
      - .actual_access:  read_only
        .address_space:  global
        .offset:         8
        .size:           8
        .value_kind:     global_buffer
      - .actual_access:  read_only
        .address_space:  global
        .offset:         16
        .size:           8
        .value_kind:     global_buffer
      - .actual_access:  read_only
        .address_space:  global
        .offset:         24
        .size:           8
        .value_kind:     global_buffer
      - .actual_access:  read_only
        .address_space:  global
        .offset:         32
        .size:           8
        .value_kind:     global_buffer
      - .actual_access:  read_only
        .address_space:  global
        .offset:         40
        .size:           8
        .value_kind:     global_buffer
      - .actual_access:  read_only
        .address_space:  global
        .offset:         48
        .size:           8
        .value_kind:     global_buffer
      - .actual_access:  read_only
        .address_space:  global
        .offset:         56
        .size:           8
        .value_kind:     global_buffer
      - .actual_access:  read_only
        .address_space:  global
        .offset:         64
        .size:           8
        .value_kind:     global_buffer
      - .actual_access:  read_only
        .address_space:  global
        .offset:         72
        .size:           8
        .value_kind:     global_buffer
      - .address_space:  global
        .offset:         80
        .size:           8
        .value_kind:     global_buffer
    .group_segment_fixed_size: 16896
    .kernarg_segment_align: 8
    .kernarg_segment_size: 88
    .language:       OpenCL C
    .language_version:
      - 2
      - 0
    .max_flat_workgroup_size: 128
    .name:           _Z11edge_kernelILi64ELb0EEvPKfS1_PKDF16_PKiS5_S1_S1_S1_S1_S1_PDF16_
    .private_segment_fixed_size: 0
    .sgpr_count:     26
    .sgpr_spill_count: 0
    .symbol:         _Z11edge_kernelILi64ELb0EEvPKfS1_PKDF16_PKiS5_S1_S1_S1_S1_S1_PDF16_.kd
    .uniform_work_group_size: 1
    .uses_dynamic_stack: false
    .vgpr_count:     176
    .vgpr_spill_count: 0
    .wavefront_size: 64
